# barrier poll back-off: grid-barrier spin loops sleep 192 cycles between polls instead of 64
# speedup vs baseline: 1.0054x; 1.0054x over previous
; __device__ __forceinline__ unsigned xb_ld(unsigned* p)              { return __hip_atomic_load(p, __ATOMIC_RELAXED, __HIP_MEMORY_SCOPE_AGENT); }
; __device__ __forceinline__ void xcd_barrier_complete(unsigned* bar, unsigned x, unsigned& nloc, unsigned& nx) {
;     const unsigned G = gridDim.x * gridDim.y * gridDim.z;
;     unsigned sum, cnt, mine, sp = 0u;
;     for (;;) {
;         sum = 0u; cnt = 0u; mine = 0u;
; #pragma unroll
;         for (unsigned j = 0; j < 16; ++j) { const unsigned c = xb_ld(&bar[XB_XCNT(j)]); sum += c; cnt += (c > 0u) ? 1u : 0u; mine = (j == x) ? c : mine; }
;         if (sum == G) break;
;         __builtin_amdgcn_s_sleep(1);
;         if ((++sp & 255u) == 0u) { if (xb_ld(&bar[XB_TMO])) break; if (sp > XB_SPIN_CAP) { atomicAdd(&bar[XB_TMO], 1u); break; } }
;     }
;     nloc = mine > 0u ? mine : 1u; nx = cnt > 0u ? cnt : 1u;
; }
.LBB0_129:
	global_load_dword v16, v17, s[62:63] offset:1024 sc1
	global_load_dword v1, v17, s[62:63] offset:1280 sc1
	global_load_dword v2, v17, s[62:63] offset:1536 sc1
	global_load_dword v3, v17, s[62:63] offset:1792 sc1
	global_load_dword v4, v17, s[62:63] offset:2048 sc1
	global_load_dword v5, v17, s[62:63] offset:2304 sc1
	global_load_dword v6, v17, s[62:63] offset:2560 sc1
	global_load_dword v7, v17, s[62:63] offset:2816 sc1
	global_load_dword v8, v17, s[62:63] offset:3072 sc1
	global_load_dword v9, v17, s[62:63] offset:3328 sc1
	global_load_dword v10, v17, s[62:63] offset:3584 sc1
	global_load_dword v11, v17, s[62:63] offset:3840 sc1
	global_load_dword v12, v17, s[0:1] sc1
	global_load_dword v13, v17, s[4:5] sc1
	global_load_dword v14, v17, s[6:7] sc1
	global_load_dword v15, v17, s[8:9] sc1
	s_mov_b64 s[10:11], -1
	s_mov_b64 s[12:13], -1
	s_waitcnt vmcnt(14)
	v_add_u32_e32 v18, v1, v16
	s_waitcnt vmcnt(13)
	v_add_u32_e32 v18, v18, v2
	s_waitcnt vmcnt(12)
	v_add_u32_e32 v18, v18, v3
	s_waitcnt vmcnt(11)
	v_add_u32_e32 v18, v18, v4
	s_waitcnt vmcnt(10)
	v_add_u32_e32 v18, v18, v5
	s_waitcnt vmcnt(9)
	v_add_u32_e32 v18, v18, v6
	s_waitcnt vmcnt(8)
	v_add_u32_e32 v18, v18, v7
	s_waitcnt vmcnt(7)
	v_add_u32_e32 v18, v18, v8
	s_waitcnt vmcnt(6)
	v_add_u32_e32 v18, v18, v9
	s_waitcnt vmcnt(5)
	v_add_u32_e32 v18, v18, v10
	s_waitcnt vmcnt(4)
	v_add_u32_e32 v18, v18, v11
	s_waitcnt vmcnt(3)
	v_add_u32_e32 v18, v18, v12
	s_waitcnt vmcnt(2)
	v_add_u32_e32 v18, v18, v13
	s_waitcnt vmcnt(1)
	v_add_u32_e32 v18, v18, v14
	s_waitcnt vmcnt(0)
	v_add_u32_e32 v18, v18, v15
	v_cmp_eq_u32_e32 vcc, s16, v18
	s_cbranch_vccnz .LBB0_128
	s_and_b32 s10, s17, 0xff
	s_cmp_eq_u32 s10, 0
	s_mov_b64 s[10:11], -1
	s_mov_b64 s[14:15], -1
	s_sleep 3
	s_cbranch_scc1 .LBB0_133
	s_and_b64 vcc, exec, s[14:15]
	s_cbranch_vccz .LBB0_128

; __device__ __forceinline__ unsigned xb_ld(unsigned* p)              { return __hip_atomic_load(p, __ATOMIC_RELAXED, __HIP_MEMORY_SCOPE_AGENT); }
; __device__ __forceinline__ unsigned xb_add(unsigned* p, unsigned v) { return __hip_atomic_fetch_add(p, v, __ATOMIC_RELAXED, __HIP_MEMORY_SCOPE_AGENT); }
; #define XB_SPIN(cond, bar) do { unsigned _sp = 0; while (cond) { __builtin_amdgcn_s_sleep(1); \
;     if ((++_sp & 255u) == 0u) { if (xb_ld(&(bar)[XB_TMO])) break; if (_sp > XB_SPIN_CAP) { atomicAdd(&(bar)[XB_TMO], 1u); break; } } } } while (0)
; __device__ __forceinline__ void xcd_barrier(const XcdBarrier& b) {
;     ...
;             const unsigned tg = og / nx;
;             if (og + 1u == (tg + 1u) * nx) xb_add(&bar[XB_TOPGEN], 1u);
;             else XB_SPIN(xb_ld(&bar[XB_TOPGEN]) == tg, bar);
;             __builtin_amdgcn_fence(__ATOMIC_ACQUIRE, "agent");
.LBB0_145:
	s_and_b32 s16, s20, 0xff
	s_mov_b64 s[14:15], -1
	s_cmp_lg_u32 s16, 0
	s_mov_b64 s[18:19], -1
	s_sleep 3
	s_cbranch_scc0 .LBB0_148
	s_and_b64 vcc, exec, s[18:19]
	s_cbranch_vccz .LBB0_144

; __device__ __forceinline__ unsigned xb_ld(unsigned* p)              { return __hip_atomic_load(p, __ATOMIC_RELAXED, __HIP_MEMORY_SCOPE_AGENT); }
; #define XB_SPIN(cond, bar) do { unsigned _sp = 0; while (cond) { __builtin_amdgcn_s_sleep(1); \
;     if ((++_sp & 255u) == 0u) { if (xb_ld(&(bar)[XB_TMO])) break; if (_sp > XB_SPIN_CAP) { atomicAdd(&(bar)[XB_TMO], 1u); break; } } } } while (0)
; __device__ __forceinline__ void xcd_barrier(const XcdBarrier& b) {
;     ...
;         } else {
;             XB_SPIN(xb_ld(&bar[XB_XGEN(b.x)]) == gen, bar);
;             __builtin_amdgcn_fence(__ATOMIC_ACQUIRE, "agent");
.LBB0_162:
	s_and_b32 s16, s22, 0xff
	s_cmp_lg_u32 s16, 0
	s_mov_b64 s[18:19], -1
	s_sleep 3
	s_cbranch_scc0 .LBB0_165
	s_mov_b64 s[20:21], -1
	s_and_b64 vcc, exec, s[18:19]
	s_cbranch_vccz .LBB0_161
